# out-projection GEMM epilogue (residual add): the 16 residual loads issued in a rolling window of 8 with counted vmcnt instead of load-wait-store per block; on top of diff prologue hoist
# speedup vs baseline: 1.0211x; 1.0211x over previous
; __device__ __forceinline__ float bflo(unsigned w) { return __uint_as_float(w << 16); }
; __device__ __forceinline__ float bfhi(unsigned w) { return __uint_as_float(w & 0xFFFF0000u); }
; __device__ __forceinline__ unsigned cvt_pk_bf16(float lo, float hi) { f32x2c v = {lo, hi}; bf16x2c b = __builtin_convertvector(v, bf16x2c); return __builtin_bit_cast(unsigned, b); }
;     __device__ __forceinline__ void operator()(const f32x4 (&acc)[2][2][4][2], const Unit& u, int wr, int wc, int fr, int fq) const {
;     ...
; #pragma unroll
;         for (int ai = 0; ai < 2; ++ai)
; #pragma unroll
;             for (int m = 0; m < 4; ++m) { const size_t ro = (size_t)(row0 + ai * HALF + m * 16) * D + col0;
; #pragma unroll
;                 for (int bj = 0; bj < 2; ++bj) { const u32x4 h = *(const u32x4*)(hb + ro + bj * HALF); const f32x4 v0 = acc[ai][bj][m][0], v1 = acc[ai][bj][m][1];
;                     u32x4 w; w.x = cvt_pk_bf16(v0[0] + ALPHA * bflo(h.x), v0[1] + ALPHA * bfhi(h.x)); w.y = cvt_pk_bf16(v0[2] + ALPHA * bflo(h.y), v0[3] + ALPHA * bfhi(h.y));
;                     w.z = cvt_pk_bf16(v1[0] + ALPHA * bflo(h.z), v1[1] + ALPHA * bfhi(h.z)); w.w = cvt_pk_bf16(v1[2] + ALPHA * bflo(h.w), v1[3] + ALPHA * bfhi(h.w));
;                     *(u32x4*)(Z + ro + bj * HALF) = w; } }
.LBB0_1007:
	v_lshl_or_b32 v130, s22, 8, v189
	s_mov_b64 s[22:23], -1
	s_cmp_lt_i32 s57, 16
	v_ashrrev_i32_e32 v131, 31, v130
	s_cbranch_scc1 .LBB0_1009
	v_add_u32_e32 v132, s9, v188
	v_ashrrev_i32_e32 v133, 31, v132
	v_lshlrev_b64 v[132:133], 10, v[132:133]
	v_lshl_add_u64 v[132:133], v[132:133], 0, v[130:131]
	v_lshlrev_b64 v[132:133], 1, v[132:133]
	v_lshl_add_u64 v[138:139], s[4:5], 0, v[132:133]
	v_lshl_add_u64 v[140:141], s[2:3], 0, v[132:133]
	v_mov_b64_e32 v[142:143], v[138:139]
	global_load_dwordx4 v[144:147], v[142:143], off
	global_load_dwordx4 v[148:151], v[142:143], off offset:256
	v_add_co_u32_e32 v142, vcc, 0x8000, v142
	s_nop 1
	v_addc_co_u32_e32 v143, vcc, 0, v143, vcc
	global_load_dwordx4 v[152:155], v[142:143], off
	global_load_dwordx4 v[156:159], v[142:143], off offset:256
	v_add_co_u32_e32 v142, vcc, 0x8000, v142
	s_nop 1
	v_addc_co_u32_e32 v143, vcc, 0, v143, vcc
	global_load_dwordx4 v[160:163], v[142:143], off
	global_load_dwordx4 v[164:167], v[142:143], off offset:256
	v_add_co_u32_e32 v142, vcc, 0x8000, v142
	s_nop 1
	v_addc_co_u32_e32 v143, vcc, 0, v143, vcc
	global_load_dwordx4 v[168:171], v[142:143], off
	global_load_dwordx4 v[172:175], v[142:143], off offset:256
	v_add_co_u32_e32 v142, vcc, 0x28000, v142
	s_nop 1
	v_addc_co_u32_e32 v143, vcc, 0, v143, vcc
	s_waitcnt vmcnt(7)
	v_lshlrev_b32_e32 v134, 16, v144
	v_and_b32_e32 v135, 0xffff0000, v144
	v_pk_fma_f32 v[134:135], v[134:135], s[88:89], v[126:127] op_sel_hi:[1,0,1]
	s_nop 0
	v_cvt_pk_bf16_f32 v144, v134, v135
	v_lshlrev_b32_e32 v134, 16, v145
	v_and_b32_e32 v135, 0xffff0000, v145
	v_pk_fma_f32 v[134:135], v[134:135], s[88:89], v[128:129] op_sel_hi:[1,0,1]
	s_nop 0
	v_cvt_pk_bf16_f32 v145, v134, v135
	v_lshlrev_b32_e32 v134, 16, v146
	v_and_b32_e32 v135, 0xffff0000, v146
	v_pk_fma_f32 v[134:135], v[134:135], s[88:89], v[122:123] op_sel_hi:[1,0,1]
	s_nop 0
	v_cvt_pk_bf16_f32 v146, v134, v135
	v_lshlrev_b32_e32 v134, 16, v147
	v_and_b32_e32 v135, 0xffff0000, v147
	v_pk_fma_f32 v[134:135], v[134:135], s[88:89], v[124:125] op_sel_hi:[1,0,1]
	s_nop 0
	v_cvt_pk_bf16_f32 v147, v134, v135
	global_store_dwordx4 v[140:141], v[144:147], off
	s_nop 1
	global_load_dwordx4 v[144:147], v[142:143], off
	s_waitcnt vmcnt(8)
	v_lshlrev_b32_e32 v134, 16, v148
	v_and_b32_e32 v135, 0xffff0000, v148
	v_pk_fma_f32 v[134:135], v[134:135], s[88:89], v[94:95] op_sel_hi:[1,0,1]
	s_nop 0
	v_cvt_pk_bf16_f32 v148, v134, v135
	v_lshlrev_b32_e32 v134, 16, v149
	v_and_b32_e32 v135, 0xffff0000, v149
	v_pk_fma_f32 v[134:135], v[134:135], s[88:89], v[96:97] op_sel_hi:[1,0,1]
	s_nop 0
	v_cvt_pk_bf16_f32 v149, v134, v135
	v_lshlrev_b32_e32 v134, 16, v150
	v_and_b32_e32 v135, 0xffff0000, v150
	v_pk_fma_f32 v[134:135], v[134:135], s[88:89], v[90:91] op_sel_hi:[1,0,1]
	s_nop 0
	v_cvt_pk_bf16_f32 v150, v134, v135
	v_lshlrev_b32_e32 v134, 16, v151
	v_and_b32_e32 v135, 0xffff0000, v151
	v_pk_fma_f32 v[134:135], v[134:135], s[88:89], v[92:93] op_sel_hi:[1,0,1]
	s_nop 0
	v_cvt_pk_bf16_f32 v151, v134, v135
	global_store_dwordx4 v[140:141], v[148:151], off offset:256
	v_add_co_u32_e32 v140, vcc, 0x8000, v140
	s_nop 1
	v_addc_co_u32_e32 v141, vcc, 0, v141, vcc
	global_load_dwordx4 v[148:151], v[142:143], off offset:256
	v_add_co_u32_e32 v142, vcc, 0x8000, v142
	s_nop 1
	v_addc_co_u32_e32 v143, vcc, 0, v143, vcc
	s_waitcnt vmcnt(9)
	v_lshlrev_b32_e32 v134, 16, v152
	v_and_b32_e32 v135, 0xffff0000, v152
	v_pk_fma_f32 v[134:135], v[134:135], s[88:89], v[118:119] op_sel_hi:[1,0,1]
	s_nop 0
	v_cvt_pk_bf16_f32 v152, v134, v135
	v_lshlrev_b32_e32 v134, 16, v153
	v_and_b32_e32 v135, 0xffff0000, v153
	v_pk_fma_f32 v[134:135], v[134:135], s[88:89], v[120:121] op_sel_hi:[1,0,1]
	s_nop 0
	v_cvt_pk_bf16_f32 v153, v134, v135
	v_lshlrev_b32_e32 v134, 16, v154
	v_and_b32_e32 v135, 0xffff0000, v154
	v_pk_fma_f32 v[134:135], v[134:135], s[88:89], v[114:115] op_sel_hi:[1,0,1]
	s_nop 0
	v_cvt_pk_bf16_f32 v154, v134, v135
	v_lshlrev_b32_e32 v134, 16, v155
	v_and_b32_e32 v135, 0xffff0000, v155
	v_pk_fma_f32 v[134:135], v[134:135], s[88:89], v[116:117] op_sel_hi:[1,0,1]
	s_nop 0
	v_cvt_pk_bf16_f32 v155, v134, v135
	global_store_dwordx4 v[140:141], v[152:155], off
	s_nop 1
	global_load_dwordx4 v[152:155], v[142:143], off
	s_waitcnt vmcnt(10)
	v_lshlrev_b32_e32 v134, 16, v156
	v_and_b32_e32 v135, 0xffff0000, v156
	v_pk_fma_f32 v[134:135], v[134:135], s[88:89], v[86:87] op_sel_hi:[1,0,1]
	s_nop 0
	v_cvt_pk_bf16_f32 v156, v134, v135
	v_lshlrev_b32_e32 v134, 16, v157
	v_and_b32_e32 v135, 0xffff0000, v157
	v_pk_fma_f32 v[134:135], v[134:135], s[88:89], v[88:89] op_sel_hi:[1,0,1]
	s_nop 0
	v_cvt_pk_bf16_f32 v157, v134, v135
	v_lshlrev_b32_e32 v134, 16, v158
	v_and_b32_e32 v135, 0xffff0000, v158
	v_pk_fma_f32 v[134:135], v[134:135], s[88:89], v[82:83] op_sel_hi:[1,0,1]
	s_nop 0
	v_cvt_pk_bf16_f32 v158, v134, v135
	v_lshlrev_b32_e32 v134, 16, v159
	v_and_b32_e32 v135, 0xffff0000, v159
	v_pk_fma_f32 v[134:135], v[134:135], s[88:89], v[84:85] op_sel_hi:[1,0,1]
	s_nop 0
	v_cvt_pk_bf16_f32 v159, v134, v135
	global_store_dwordx4 v[140:141], v[156:159], off offset:256
	v_add_co_u32_e32 v140, vcc, 0x8000, v140
	s_nop 1
	v_addc_co_u32_e32 v141, vcc, 0, v141, vcc
	global_load_dwordx4 v[156:159], v[142:143], off offset:256
	v_add_co_u32_e32 v142, vcc, 0x8000, v142
	s_nop 1
	v_addc_co_u32_e32 v143, vcc, 0, v143, vcc
	s_waitcnt vmcnt(11)
; __device__ __forceinline__ float bflo(unsigned w) { return __uint_as_float(w << 16); }
; __device__ __forceinline__ float bfhi(unsigned w) { return __uint_as_float(w & 0xFFFF0000u); }
; __device__ __forceinline__ unsigned cvt_pk_bf16(float lo, float hi) { f32x2c v = {lo, hi}; bf16x2c b = __builtin_convertvector(v, bf16x2c); return __builtin_bit_cast(unsigned, b); }
;     __device__ __forceinline__ void operator()(const f32x4 (&acc)[2][2][4][2], const Unit& u, int wr, int wc, int fr, int fq) const {
;     ...
; #pragma unroll
;         for (int ai = 0; ai < 2; ++ai)
; #pragma unroll
;             for (int m = 0; m < 4; ++m) { const size_t ro = (size_t)(row0 + ai * HALF + m * 16) * D + col0;
; #pragma unroll
;                 for (int bj = 0; bj < 2; ++bj) { const u32x4 h = *(const u32x4*)(hb + ro + bj * HALF); const f32x4 v0 = acc[ai][bj][m][0], v1 = acc[ai][bj][m][1];
;                     u32x4 w; w.x = cvt_pk_bf16(v0[0] + ALPHA * bflo(h.x), v0[1] + ALPHA * bfhi(h.x)); w.y = cvt_pk_bf16(v0[2] + ALPHA * bflo(h.y), v0[3] + ALPHA * bfhi(h.y));
;                     w.z = cvt_pk_bf16(v1[0] + ALPHA * bflo(h.z), v1[1] + ALPHA * bfhi(h.z)); w.w = cvt_pk_bf16(v1[2] + ALPHA * bflo(h.w), v1[3] + ALPHA * bfhi(h.w));
;                     *(u32x4*)(Z + ro + bj * HALF) = w; } }
	v_lshlrev_b32_e32 v134, 16, v160
	v_and_b32_e32 v135, 0xffff0000, v160
	v_pk_fma_f32 v[134:135], v[134:135], s[88:89], v[110:111] op_sel_hi:[1,0,1]
	s_nop 0
	v_cvt_pk_bf16_f32 v160, v134, v135
	v_lshlrev_b32_e32 v134, 16, v161
	v_and_b32_e32 v135, 0xffff0000, v161
	v_pk_fma_f32 v[134:135], v[134:135], s[88:89], v[112:113] op_sel_hi:[1,0,1]
	s_nop 0
	v_cvt_pk_bf16_f32 v161, v134, v135
	v_lshlrev_b32_e32 v134, 16, v162
	v_and_b32_e32 v135, 0xffff0000, v162
	v_pk_fma_f32 v[134:135], v[134:135], s[88:89], v[106:107] op_sel_hi:[1,0,1]
	s_nop 0
	v_cvt_pk_bf16_f32 v162, v134, v135
	v_lshlrev_b32_e32 v134, 16, v163
	v_and_b32_e32 v135, 0xffff0000, v163
	v_pk_fma_f32 v[134:135], v[134:135], s[88:89], v[108:109] op_sel_hi:[1,0,1]
	s_nop 0
	v_cvt_pk_bf16_f32 v163, v134, v135
	global_store_dwordx4 v[140:141], v[160:163], off
	s_nop 1
	global_load_dwordx4 v[160:163], v[142:143], off
	s_waitcnt vmcnt(12)
	v_lshlrev_b32_e32 v134, 16, v164
	v_and_b32_e32 v135, 0xffff0000, v164
	v_pk_fma_f32 v[134:135], v[134:135], s[88:89], v[78:79] op_sel_hi:[1,0,1]
	s_nop 0
	v_cvt_pk_bf16_f32 v164, v134, v135
	v_lshlrev_b32_e32 v134, 16, v165
	v_and_b32_e32 v135, 0xffff0000, v165
	v_pk_fma_f32 v[134:135], v[134:135], s[88:89], v[80:81] op_sel_hi:[1,0,1]
	s_nop 0
	v_cvt_pk_bf16_f32 v165, v134, v135
	v_lshlrev_b32_e32 v134, 16, v166
	v_and_b32_e32 v135, 0xffff0000, v166
	v_pk_fma_f32 v[134:135], v[134:135], s[88:89], v[74:75] op_sel_hi:[1,0,1]
	s_nop 0
	v_cvt_pk_bf16_f32 v166, v134, v135
	v_lshlrev_b32_e32 v134, 16, v167
	v_and_b32_e32 v135, 0xffff0000, v167
	v_pk_fma_f32 v[134:135], v[134:135], s[88:89], v[76:77] op_sel_hi:[1,0,1]
	s_nop 0
	v_cvt_pk_bf16_f32 v167, v134, v135
	global_store_dwordx4 v[140:141], v[164:167], off offset:256
	v_add_co_u32_e32 v140, vcc, 0x8000, v140
	s_nop 1
	v_addc_co_u32_e32 v141, vcc, 0, v141, vcc
	global_load_dwordx4 v[164:167], v[142:143], off offset:256
	v_add_co_u32_e32 v142, vcc, 0x8000, v142
	s_nop 1
	v_addc_co_u32_e32 v143, vcc, 0, v143, vcc
	s_waitcnt vmcnt(13)
	v_lshlrev_b32_e32 v134, 16, v168
	v_and_b32_e32 v135, 0xffff0000, v168
	v_pk_fma_f32 v[134:135], v[134:135], s[88:89], v[102:103] op_sel_hi:[1,0,1]
	s_nop 0
	v_cvt_pk_bf16_f32 v168, v134, v135
	v_lshlrev_b32_e32 v134, 16, v169
	v_and_b32_e32 v135, 0xffff0000, v169
	v_pk_fma_f32 v[134:135], v[134:135], s[88:89], v[104:105] op_sel_hi:[1,0,1]
	s_nop 0
	v_cvt_pk_bf16_f32 v169, v134, v135
	v_lshlrev_b32_e32 v134, 16, v170
	v_and_b32_e32 v135, 0xffff0000, v170
	v_pk_fma_f32 v[134:135], v[134:135], s[88:89], v[98:99] op_sel_hi:[1,0,1]
	s_nop 0
	v_cvt_pk_bf16_f32 v170, v134, v135
	v_lshlrev_b32_e32 v134, 16, v171
	v_and_b32_e32 v135, 0xffff0000, v171
	v_pk_fma_f32 v[134:135], v[134:135], s[88:89], v[100:101] op_sel_hi:[1,0,1]
	s_nop 0
	v_cvt_pk_bf16_f32 v171, v134, v135
	global_store_dwordx4 v[140:141], v[168:171], off
	s_nop 1
	global_load_dwordx4 v[168:171], v[142:143], off
	s_waitcnt vmcnt(14)
	v_lshlrev_b32_e32 v134, 16, v172
	v_and_b32_e32 v135, 0xffff0000, v172
	v_pk_fma_f32 v[134:135], v[134:135], s[88:89], v[70:71] op_sel_hi:[1,0,1]
	s_nop 0
	v_cvt_pk_bf16_f32 v172, v134, v135
	v_lshlrev_b32_e32 v134, 16, v173
	v_and_b32_e32 v135, 0xffff0000, v173
	v_pk_fma_f32 v[134:135], v[134:135], s[88:89], v[72:73] op_sel_hi:[1,0,1]
	s_nop 0
	v_cvt_pk_bf16_f32 v173, v134, v135
	v_lshlrev_b32_e32 v134, 16, v174
	v_and_b32_e32 v135, 0xffff0000, v174
	v_pk_fma_f32 v[134:135], v[134:135], s[88:89], v[66:67] op_sel_hi:[1,0,1]
	s_nop 0
	v_cvt_pk_bf16_f32 v174, v134, v135
	v_lshlrev_b32_e32 v134, 16, v175
	v_and_b32_e32 v135, 0xffff0000, v175
	v_pk_fma_f32 v[134:135], v[134:135], s[88:89], v[68:69] op_sel_hi:[1,0,1]
	s_nop 0
	v_cvt_pk_bf16_f32 v175, v134, v135
	global_store_dwordx4 v[140:141], v[172:175], off offset:256
	v_add_co_u32_e32 v140, vcc, 0x28000, v140
	s_nop 1
	v_addc_co_u32_e32 v141, vcc, 0, v141, vcc
	global_load_dwordx4 v[172:175], v[142:143], off offset:256
	s_waitcnt vmcnt(14)
	v_lshlrev_b32_e32 v134, 16, v144
	v_and_b32_e32 v135, 0xffff0000, v144
	v_pk_fma_f32 v[134:135], v[134:135], s[88:89], v[62:63] op_sel_hi:[1,0,1]
	s_nop 0
	v_cvt_pk_bf16_f32 v144, v134, v135
	v_lshlrev_b32_e32 v134, 16, v145
	v_and_b32_e32 v135, 0xffff0000, v145
	v_pk_fma_f32 v[134:135], v[134:135], s[88:89], v[64:65] op_sel_hi:[1,0,1]
	s_nop 0
	v_cvt_pk_bf16_f32 v145, v134, v135
	v_lshlrev_b32_e32 v134, 16, v146
	v_and_b32_e32 v135, 0xffff0000, v146
	v_pk_fma_f32 v[134:135], v[134:135], s[88:89], v[58:59] op_sel_hi:[1,0,1]
	s_nop 0
	v_cvt_pk_bf16_f32 v146, v134, v135
	v_lshlrev_b32_e32 v134, 16, v147
	v_and_b32_e32 v135, 0xffff0000, v147
	v_pk_fma_f32 v[134:135], v[134:135], s[88:89], v[60:61] op_sel_hi:[1,0,1]
	s_nop 0
	v_cvt_pk_bf16_f32 v147, v134, v135
	global_store_dwordx4 v[140:141], v[144:147], off
	s_nop 1
	s_waitcnt vmcnt(13)
	v_lshlrev_b32_e32 v134, 16, v148
	v_and_b32_e32 v135, 0xffff0000, v148
	v_pk_fma_f32 v[134:135], v[134:135], s[88:89], v[46:47] op_sel_hi:[1,0,1]
	s_nop 0
	v_cvt_pk_bf16_f32 v148, v134, v135
	v_lshlrev_b32_e32 v134, 16, v149
	v_and_b32_e32 v135, 0xffff0000, v149
	v_pk_fma_f32 v[134:135], v[134:135], s[88:89], v[48:49] op_sel_hi:[1,0,1]
	s_nop 0
	v_cvt_pk_bf16_f32 v149, v134, v135
	v_lshlrev_b32_e32 v134, 16, v150
	v_and_b32_e32 v135, 0xffff0000, v150
	v_pk_fma_f32 v[134:135], v[134:135], s[88:89], v[38:39] op_sel_hi:[1,0,1]
	s_nop 0
	v_cvt_pk_bf16_f32 v150, v134, v135
	v_lshlrev_b32_e32 v134, 16, v151
	v_and_b32_e32 v135, 0xffff0000, v151
	v_pk_fma_f32 v[134:135], v[134:135], s[88:89], v[40:41] op_sel_hi:[1,0,1]
	s_nop 0
	v_cvt_pk_bf16_f32 v151, v134, v135
	global_store_dwordx4 v[140:141], v[148:151], off offset:256
	v_add_co_u32_e32 v140, vcc, 0x8000, v140
	s_nop 1
	v_addc_co_u32_e32 v141, vcc, 0, v141, vcc
	s_waitcnt vmcnt(12)
; __device__ __forceinline__ float bflo(unsigned w) { return __uint_as_float(w << 16); }
; __device__ __forceinline__ float bfhi(unsigned w) { return __uint_as_float(w & 0xFFFF0000u); }
; __device__ __forceinline__ unsigned cvt_pk_bf16(float lo, float hi) { f32x2c v = {lo, hi}; bf16x2c b = __builtin_convertvector(v, bf16x2c); return __builtin_bit_cast(unsigned, b); }
;     __device__ __forceinline__ void operator()(const f32x4 (&acc)[2][2][4][2], const Unit& u, int wr, int wc, int fr, int fq) const {
;     ...
; #pragma unroll
;         for (int ai = 0; ai < 2; ++ai)
; #pragma unroll
;             for (int m = 0; m < 4; ++m) { const size_t ro = (size_t)(row0 + ai * HALF + m * 16) * D + col0;
; #pragma unroll
;                 for (int bj = 0; bj < 2; ++bj) { const u32x4 h = *(const u32x4*)(hb + ro + bj * HALF); const f32x4 v0 = acc[ai][bj][m][0], v1 = acc[ai][bj][m][1];
;                     u32x4 w; w.x = cvt_pk_bf16(v0[0] + ALPHA * bflo(h.x), v0[1] + ALPHA * bfhi(h.x)); w.y = cvt_pk_bf16(v0[2] + ALPHA * bflo(h.y), v0[3] + ALPHA * bfhi(h.y));
;                     w.z = cvt_pk_bf16(v1[0] + ALPHA * bflo(h.z), v1[1] + ALPHA * bfhi(h.z)); w.w = cvt_pk_bf16(v1[2] + ALPHA * bflo(h.w), v1[3] + ALPHA * bfhi(h.w));
;                     *(u32x4*)(Z + ro + bj * HALF) = w; } }
	v_lshlrev_b32_e32 v134, 16, v152
	v_and_b32_e32 v135, 0xffff0000, v152
	v_pk_fma_f32 v[134:135], v[134:135], s[88:89], v[54:55] op_sel_hi:[1,0,1]
	s_nop 0
	v_cvt_pk_bf16_f32 v152, v134, v135
	v_lshlrev_b32_e32 v134, 16, v153
	v_and_b32_e32 v135, 0xffff0000, v153
	v_pk_fma_f32 v[134:135], v[134:135], s[88:89], v[56:57] op_sel_hi:[1,0,1]
	s_nop 0
	v_cvt_pk_bf16_f32 v153, v134, v135
	v_lshlrev_b32_e32 v134, 16, v154
	v_and_b32_e32 v135, 0xffff0000, v154
	v_pk_fma_f32 v[134:135], v[134:135], s[88:89], v[50:51] op_sel_hi:[1,0,1]
	s_nop 0
	v_cvt_pk_bf16_f32 v154, v134, v135
	v_lshlrev_b32_e32 v134, 16, v155
	v_and_b32_e32 v135, 0xffff0000, v155
	v_pk_fma_f32 v[134:135], v[134:135], s[88:89], v[52:53] op_sel_hi:[1,0,1]
	s_nop 0
	v_cvt_pk_bf16_f32 v155, v134, v135
	global_store_dwordx4 v[140:141], v[152:155], off
	s_nop 1
	s_waitcnt vmcnt(11)
	v_lshlrev_b32_e32 v134, 16, v156
	v_and_b32_e32 v135, 0xffff0000, v156
	v_pk_fma_f32 v[134:135], v[134:135], s[88:89], v[30:31] op_sel_hi:[1,0,1]
	s_nop 0
	v_cvt_pk_bf16_f32 v156, v134, v135
	v_lshlrev_b32_e32 v134, 16, v157
	v_and_b32_e32 v135, 0xffff0000, v157
	v_pk_fma_f32 v[134:135], v[134:135], s[88:89], v[32:33] op_sel_hi:[1,0,1]
	s_nop 0
	v_cvt_pk_bf16_f32 v157, v134, v135
	v_lshlrev_b32_e32 v134, 16, v158
	v_and_b32_e32 v135, 0xffff0000, v158
	v_pk_fma_f32 v[134:135], v[134:135], s[88:89], v[22:23] op_sel_hi:[1,0,1]
	s_nop 0
	v_cvt_pk_bf16_f32 v158, v134, v135
	v_lshlrev_b32_e32 v134, 16, v159
	v_and_b32_e32 v135, 0xffff0000, v159
	v_pk_fma_f32 v[134:135], v[134:135], s[88:89], v[24:25] op_sel_hi:[1,0,1]
	s_nop 0
	v_cvt_pk_bf16_f32 v159, v134, v135
	global_store_dwordx4 v[140:141], v[156:159], off offset:256
	v_add_co_u32_e32 v140, vcc, 0x8000, v140
	s_nop 1
	v_addc_co_u32_e32 v141, vcc, 0, v141, vcc
	s_waitcnt vmcnt(10)
	v_lshlrev_b32_e32 v134, 16, v160
	v_and_b32_e32 v135, 0xffff0000, v160
	v_pk_fma_f32 v[134:135], v[134:135], s[88:89], v[42:43] op_sel_hi:[1,0,1]
	s_nop 0
	v_cvt_pk_bf16_f32 v160, v134, v135
	v_lshlrev_b32_e32 v134, 16, v161
	v_and_b32_e32 v135, 0xffff0000, v161
	v_pk_fma_f32 v[134:135], v[134:135], s[88:89], v[44:45] op_sel_hi:[1,0,1]
	s_nop 0
	v_cvt_pk_bf16_f32 v161, v134, v135
	v_lshlrev_b32_e32 v134, 16, v162
	v_and_b32_e32 v135, 0xffff0000, v162
	v_pk_fma_f32 v[134:135], v[134:135], s[88:89], v[34:35] op_sel_hi:[1,0,1]
	s_nop 0
	v_cvt_pk_bf16_f32 v162, v134, v135
	v_lshlrev_b32_e32 v134, 16, v163
	v_and_b32_e32 v135, 0xffff0000, v163
	v_pk_fma_f32 v[134:135], v[134:135], s[88:89], v[36:37] op_sel_hi:[1,0,1]
	s_nop 0
	v_cvt_pk_bf16_f32 v163, v134, v135
	global_store_dwordx4 v[140:141], v[160:163], off
	s_nop 1
	s_waitcnt vmcnt(9)
	v_lshlrev_b32_e32 v134, 16, v164
	v_and_b32_e32 v135, 0xffff0000, v164
	v_pk_fma_f32 v[134:135], v[134:135], s[88:89], v[14:15] op_sel_hi:[1,0,1]
	s_nop 0
	v_cvt_pk_bf16_f32 v164, v134, v135
	v_lshlrev_b32_e32 v134, 16, v165
	v_and_b32_e32 v135, 0xffff0000, v165
	v_pk_fma_f32 v[134:135], v[134:135], s[88:89], v[16:17] op_sel_hi:[1,0,1]
	s_nop 0
	v_cvt_pk_bf16_f32 v165, v134, v135
	v_lshlrev_b32_e32 v134, 16, v166
	v_and_b32_e32 v135, 0xffff0000, v166
	v_pk_fma_f32 v[134:135], v[134:135], s[88:89], v[10:11] op_sel_hi:[1,0,1]
	s_nop 0
	v_cvt_pk_bf16_f32 v166, v134, v135
	v_lshlrev_b32_e32 v134, 16, v167
	v_and_b32_e32 v135, 0xffff0000, v167
	v_pk_fma_f32 v[134:135], v[134:135], s[88:89], v[12:13] op_sel_hi:[1,0,1]
	s_nop 0
	v_cvt_pk_bf16_f32 v167, v134, v135
	global_store_dwordx4 v[140:141], v[164:167], off offset:256
	v_add_co_u32_e32 v140, vcc, 0x8000, v140
	s_nop 1
	v_addc_co_u32_e32 v141, vcc, 0, v141, vcc
	s_waitcnt vmcnt(8)
	v_lshlrev_b32_e32 v134, 16, v168
	v_and_b32_e32 v135, 0xffff0000, v168
	v_pk_fma_f32 v[134:135], v[134:135], s[88:89], v[26:27] op_sel_hi:[1,0,1]
	s_nop 0
	v_cvt_pk_bf16_f32 v168, v134, v135
	v_lshlrev_b32_e32 v134, 16, v169
	v_and_b32_e32 v135, 0xffff0000, v169
	v_pk_fma_f32 v[134:135], v[134:135], s[88:89], v[28:29] op_sel_hi:[1,0,1]
	s_nop 0
	v_cvt_pk_bf16_f32 v169, v134, v135
	v_lshlrev_b32_e32 v134, 16, v170
	v_and_b32_e32 v135, 0xffff0000, v170
	v_pk_fma_f32 v[134:135], v[134:135], s[88:89], v[18:19] op_sel_hi:[1,0,1]
	s_nop 0
	v_cvt_pk_bf16_f32 v170, v134, v135
	v_lshlrev_b32_e32 v134, 16, v171
	v_and_b32_e32 v135, 0xffff0000, v171
	v_pk_fma_f32 v[134:135], v[134:135], s[88:89], v[20:21] op_sel_hi:[1,0,1]
	s_nop 0
	v_cvt_pk_bf16_f32 v171, v134, v135
	global_store_dwordx4 v[140:141], v[168:171], off
	s_nop 1
	s_waitcnt vmcnt(7)
	v_lshlrev_b32_e32 v134, 16, v172
	v_and_b32_e32 v135, 0xffff0000, v172
	v_pk_fma_f32 v[134:135], v[134:135], s[88:89], v[6:7] op_sel_hi:[1,0,1]
	s_nop 0
	v_cvt_pk_bf16_f32 v172, v134, v135
	v_lshlrev_b32_e32 v134, 16, v173
	v_and_b32_e32 v135, 0xffff0000, v173
	v_pk_fma_f32 v[134:135], v[134:135], s[88:89], v[8:9] op_sel_hi:[1,0,1]
	s_nop 0
	v_cvt_pk_bf16_f32 v173, v134, v135
	v_lshlrev_b32_e32 v134, 16, v174
	v_and_b32_e32 v135, 0xffff0000, v174
	v_pk_fma_f32 v[134:135], v[134:135], s[88:89], v[2:3] op_sel_hi:[1,0,1]
	s_nop 0
	v_cvt_pk_bf16_f32 v174, v134, v135
	v_lshlrev_b32_e32 v134, 16, v175
	v_and_b32_e32 v135, 0xffff0000, v175
	v_pk_fma_f32 v[134:135], v[134:135], s[88:89], v[4:5] op_sel_hi:[1,0,1]
	s_nop 0
	v_cvt_pk_bf16_f32 v175, v134, v135
	global_store_dwordx4 v[140:141], v[172:175], off offset:256
	s_nop 1
	s_mov_b64 s[22:23], 0
